# phase-0 tail: cache lines of the eight small parameter vectors read by the serial scalar loops (last workgroup, thread 0) touched up front behind one wait
# speedup vs baseline: 1.0029x; 1.0028x over previous
; __device__ __forceinline__ void ph_prologue(const Ptrs& P, unsigned char* lds, unsigned& sacc) {
;     ...
;     if ((int)blockIdx.x == G - 1 && threadIdx.x == 0) {
;         float* sc = (float*)(ws + WS_SCAL);
;         float mq = 0, mk = 0;
;         for (int i = 0; i < 192; ++i) { mq = fmaxf(mq, fabsf(P.in[21][i])); mk = fmaxf(mk, fabsf(P.in[22][i])); }
;         sc[0] = sqrtf(192.f) * mq * mk * LOG2E;
;         mq = 0; mk = 0;
;         for (int i = 0; i < 64; ++i) { mq = fmaxf(mq, fabsf(P.in[25][i])); mk = fmaxf(mk, fabsf(P.in[26][i])); }
;         sc[1] = 8.f * mq * mk * LOG2E;
;         float s1 = 0, s2 = 0;
;         for (int i = 0; i < 64; ++i) { s1 += P.in[27][i] * P.in[28][i]; s2 += P.in[29][i] * P.in[30][i]; }
.LBB0_612:
	s_add_i32 s0, s62, -1
	s_cmp_eq_u32 s2, s0
	v_readlane_b32 s4, v254, 22
	s_cselect_b64 s[0:1], -1, 0
	v_readlane_b32 s5, v254, 23
	s_and_b64 s[4:5], s[4:5], s[0:1]
	s_and_saveexec_b64 s[0:1], s[4:5]
	s_cbranch_execz .LBB0_620
	s_mov_b64 s[4:5], 0
	v_mov_b32_e32 v2, 0
	v_mov_b32_e32 v3, 0
	v_mov_b32_e32 v4, 0
	v_readlane_b32 s82, v254, 5
	v_readlane_b32 s83, v254, 6
	v_readlane_b32 s84, v254, 7
	v_readlane_b32 s85, v254, 8
	v_readlane_b32 s86, v254, 9
	v_readlane_b32 s87, v254, 10
	v_readlane_b32 s88, v254, 11
	v_readlane_b32 s89, v254, 12
	v_readlane_b32 s90, v254, 13
	v_readlane_b32 s91, v254, 14
	v_readlane_b32 s92, v254, 15
	v_readlane_b32 s93, v254, 16
	global_load_dword v5, v2, s[22:23]
	global_load_dword v5, v2, s[22:23] offset:128
	global_load_dword v5, v2, s[22:23] offset:256
	global_load_dword v5, v2, s[22:23] offset:384
	global_load_dword v5, v2, s[22:23] offset:512
	global_load_dword v5, v2, s[22:23] offset:640
	global_load_dword v5, v2, s[22:23] offset:764
	global_load_dword v5, v2, s[24:25]
	global_load_dword v5, v2, s[24:25] offset:128
	global_load_dword v5, v2, s[24:25] offset:256
	global_load_dword v5, v2, s[24:25] offset:384
	global_load_dword v5, v2, s[24:25] offset:512
	global_load_dword v5, v2, s[24:25] offset:640
	global_load_dword v5, v2, s[24:25] offset:764
	global_load_dword v5, v2, s[82:83]
	global_load_dword v5, v2, s[82:83] offset:128
	global_load_dword v5, v2, s[82:83] offset:252
	global_load_dword v5, v2, s[84:85]
	global_load_dword v5, v2, s[84:85] offset:128
	global_load_dword v5, v2, s[84:85] offset:252
	global_load_dword v5, v2, s[86:87]
	global_load_dword v5, v2, s[86:87] offset:128
	global_load_dword v5, v2, s[86:87] offset:252
	global_load_dword v5, v2, s[88:89]
	global_load_dword v5, v2, s[88:89] offset:128
	global_load_dword v5, v2, s[88:89] offset:252
	global_load_dword v5, v2, s[90:91]
	global_load_dword v5, v2, s[90:91] offset:128
	global_load_dword v5, v2, s[90:91] offset:252
	global_load_dword v5, v2, s[92:93]
	global_load_dword v5, v2, s[92:93] offset:128
	global_load_dword v5, v2, s[92:93] offset:252
	s_waitcnt vmcnt(0)
